# baseline (speedup 1.0000x reference)
.LBB2_4:
	s_or_b64 exec, exec, s[4:5]
	s_load_dwordx16 s[36:51], s[0:1], 0x30
	s_load_dwordx4 s[52:55], s[0:1], 0xb0
	s_add_i32 s0, 0, 0x20808
	v_mov_b32_e32 v2, s0
	s_waitcnt lgkmcnt(0)
	s_barrier
	ds_read_b32 v2, v2
	v_writelane_b32 v244, s52, 2
	s_brev_b32 s62, 64
	s_mov_b32 s60, s28
	v_writelane_b32 v244, s53, 3
	s_waitcnt lgkmcnt(0)
	v_readfirstlane_b32 s0, v2
	s_ashr_i32 s1, s0, 31
	v_writelane_b32 v244, s54, 4
	s_lshl_b64 s[2:3], s[0:1], 2
	v_writelane_b32 v244, s55, 5
	s_add_u32 s78, s10, s2
	s_addc_u32 s79, s11, s3
	v_readlane_b32 s2, v244, 0
	v_readlane_b32 s3, v244, 1
	s_and_b32 s53, s41, 0xffff
	s_and_b32 s61, s29, 0xffff
	s_and_b32 s65, s27, 0xffff
	s_and_b32 s69, s3, 0xffff
	s_add_u32 s4, s24, 0x80
	s_addc_u32 s5, s25, 0
	v_writelane_b32 v244, s4, 6
	s_mov_b32 s55, 0x20000
	s_mov_b32 s54, 0x90000
	v_writelane_b32 v244, s5, 7
	s_add_u32 s4, s24, 0xf80
	s_addc_u32 s5, s25, 0
	s_and_b32 s3, s0, 7
	s_add_i32 s76, 0, 0x20800
	s_lshl_b32 s1, s3, 2
	v_writelane_b32 v244, s4, 8
	s_add_i32 s77, s76, s1
	s_lshl_b32 s1, s3, 8
	v_writelane_b32 v244, s5, 9
	s_or_b32 s1, s1, 0x5000000
	v_writelane_b32 v244, s1, 10
	s_add_i32 s1, s0, 1
	s_and_b32 s4, s1, 7
	s_lshl_b32 s1, s4, 2
	s_and_b32 s73, s31, 0xffff
	s_add_i32 s5, s76, s1
	s_add_u32 s34, s10, s1
	v_writelane_b32 v244, s5, 11
	s_addc_u32 s35, s11, 0
	v_writelane_b32 v244, s34, 12
	s_lshl_b32 s1, s4, 8
	s_or_b32 s1, s1, 0x5000000
	v_writelane_b32 v244, s35, 13
	v_writelane_b32 v244, s4, 14
	v_writelane_b32 v244, s1, 15
	s_add_i32 s1, s0, 2
	s_and_b32 s4, s1, 7
	s_lshl_b32 s1, s4, 2
	s_add_i32 s5, s76, s1
	s_add_u32 s34, s10, s1
	v_writelane_b32 v244, s5, 16
	s_addc_u32 s35, s11, 0
	v_writelane_b32 v244, s34, 17
	s_lshl_b32 s1, s4, 8
	s_or_b32 s1, s1, 0x5000000
	v_writelane_b32 v244, s35, 18
	v_writelane_b32 v244, s4, 19
	v_writelane_b32 v244, s1, 20
	s_add_i32 s1, s0, 3
	s_and_b32 s4, s1, 7
	s_lshl_b32 s1, s4, 2
	s_add_i32 s5, s76, s1
	s_add_u32 s34, s10, s1
	v_writelane_b32 v244, s5, 21
	s_addc_u32 s35, s11, 0
	v_writelane_b32 v244, s34, 22
	s_lshl_b32 s1, s4, 8
	s_or_b32 s1, s1, 0x5000000
	v_writelane_b32 v244, s35, 23
	v_writelane_b32 v244, s4, 24
	v_writelane_b32 v244, s1, 25
	v_writelane_b32 v244, s3, 26
	s_xor_b32 s3, s3, 4
	s_lshl_b32 s1, s3, 2
	s_add_i32 s4, s76, s1
	v_writelane_b32 v244, s4, 27
	s_add_u32 s4, s10, s1
	s_addc_u32 s5, s11, 0
	v_writelane_b32 v244, s4, 28
	s_lshl_b32 s1, s3, 8
	s_or_b32 s1, s1, 0x5000000
	v_writelane_b32 v244, s5, 29
	v_writelane_b32 v244, s3, 30
	v_writelane_b32 v244, s1, 31
	s_add_i32 s1, s0, 5
	s_and_b32 s3, s1, 7
	s_lshl_b32 s1, s3, 2
	s_add_i32 s4, s76, s1
	v_writelane_b32 v244, s4, 32
	s_add_u32 s4, s10, s1
	s_addc_u32 s5, s11, 0
	v_writelane_b32 v244, s4, 33
	s_lshl_b32 s1, s3, 8
	s_or_b32 s1, s1, 0x5000000
	v_writelane_b32 v244, s5, 34
	v_writelane_b32 v244, s3, 35
	v_writelane_b32 v244, s1, 36
	s_add_i32 s1, s0, 6
	s_and_b32 s3, s1, 7
	s_lshl_b32 s1, s3, 2
	s_add_i32 s4, s76, s1
	v_writelane_b32 v244, s4, 37
	s_add_u32 s4, s10, s1
	s_addc_u32 s5, s11, 0
	v_writelane_b32 v244, s4, 38
	s_mov_b32 s52, s40
	s_mov_b32 s63, s55
	v_writelane_b32 v244, s5, 39
	s_mov_b32 s67, s55
	s_mov_b32 s71, s55
	v_writelane_b32 v244, s52, 40
	s_lshl_b32 s1, s3, 8
	s_add_i32 s0, s0, -1
	v_writelane_b32 v244, s53, 41
	v_writelane_b32 v244, s54, 42
	v_writelane_b32 v244, s55, 43
	v_writelane_b32 v244, s3, 44
	s_or_b32 s1, s1, 0x5000000
	v_writelane_b32 v244, s1, 45
	s_and_b32 s1, s0, 7
	s_lshl_b32 s0, s1, 2
	s_mov_b32 s68, s2
	s_add_i32 s2, s76, s0
	v_writelane_b32 v244, s2, 46
	s_add_u32 s2, s10, s0
	s_addc_u32 s3, s11, 0
	v_writelane_b32 v244, s2, 47
	s_lshl_b32 s0, s1, 8
	s_or_b32 s0, s0, 0x5000000
	v_writelane_b32 v244, s3, 48
	v_writelane_b32 v244, s1, 49
	v_writelane_b32 v244, s0, 50
	s_add_i32 s0, 0, 0x20884
	v_writelane_b32 v244, s0, 51
	s_add_i32 s0, 0, 0x20880
	v_writelane_b32 v244, s0, 52
	s_mov_b32 s1, 0
	s_brev_b32 s66, 32
	s_mov_b32 s64, s26
	s_mov_b32 s70, 0x4800000
	s_mov_b32 s74, 0x2400000
	s_mov_b32 s75, s55
	s_mov_b32 s72, s30
	v_mov_b32_e32 v163, 0
	v_mov_b32_e32 v182, 0xfffff000
	v_mov_b32_e32 v183, 1
	s_add_i32 s85, 0, 0x20804
	v_writelane_b32 v244, s0, 53
	s_nop 1
	v_writelane_b32 v244, s1, 54
	v_writelane_b32 v244, s1, 55
	s_branch .LBB2_7

.LBB2_6:
.LBB2_7:
	s_barrier
	s_and_saveexec_b64 s[2:3], s[6:7]
	s_cbranch_execz .LBB2_270
	v_add_u32_e32 v1, v245, v1
	s_sub_u32 s53, s77, s76
	s_lshr_b32 s53, s53, 2
	s_lshl_b32 s0, s53, 2
	s_sub_u32 s56, s78, s0
	s_subb_u32 s57, s79, 0
	v_readlane_b32 s54, v244, 55
	v_readfirstlane_b32 s52, v1
	s_cmp_lg_u32 s54, 0
	s_cbranch_scc1 .Lsched_cmb
	v_mov_b32_e32 v2, s77
	ds_read_b32 v2, v2 offset:32
	s_waitcnt lgkmcnt(0)
	v_readfirstlane_b32 s33, v2
	s_mul_i32 s34, s33, 17
	s_addk_i32 s34, 0x30
	s_mov_b32 s55, s53
	s_cmp_lt_i32 s52, s34
	s_cbranch_scc1 .Lsched_decode
	s_mov_b64 exec, 0xff
	v_lshlrev_b32_e32 v2, 2, v0
	global_load_dword v3, v2, s[56:57] sc1
	v_add_u32_e32 v4, s76, v2
	ds_read_b32 v5, v4 offset:32
	s_waitcnt vmcnt(0) lgkmcnt(0)
	v_mul_u32_u24_e32 v4, 17, v5
	v_add_u32_e32 v4, 48, v4
	v_cmp_lt_i32_e32 vcc, v3, v4
	s_nop 1
	s_and_b32 s35, vcc_lo, 0xff
	s_mov_b64 exec, 1
	s_add_u32 s1, s53, 1
	s_and_b32 s1, s1, 7
.Lsched_pick:
	s_lshl_b32 s0, s35, 8
	s_or_b32 s0, s0, s35
	s_lshr_b32 s0, s0, s1
	s_and_b32 s0, s0, 0xff
	s_cmp_eq_u32 s0, 0
	s_cbranch_scc1 .Lsched_nowork
	s_ff1_i32_b32 s0, s0
	s_add_u32 s55, s0, s1
	s_and_b32 s55, s55, 7
	s_nop 3
	v_readlane_b32 s33, v5, s55
	s_mul_i32 s34, s33, 17
	s_addk_i32 s34, 0x30
	s_lshl_b32 s0, s55, 2
	v_mov_b32_e32 v2, s0
	v_mov_b32_e32 v3, 1
	global_atomic_add v3, v2, v3, s[56:57] sc0
	s_waitcnt vmcnt(0)
	v_readfirstlane_b32 s52, v3
	s_cmp_lt_i32 s52, s34
	s_cbranch_scc1 .Lsched_decode
	s_lshl_b32 s0, 1, s55
	s_andn2_b32 s35, s35, s0
	s_branch .Lsched_pick
.Lsched_nowork:
	s_mov_b32 s54, 1
	v_writelane_b32 v244, s54, 55
.Lsched_cmb:
	v_mov_b32_e32 v2, 32
	v_mov_b32_e32 v3, 1
	global_atomic_add v3, v2, v3, s[56:57] sc0
	s_waitcnt vmcnt(0)
	v_readfirstlane_b32 s52, v3
	s_mov_b32 s55, 0
	s_mov_b32 s35, -1
	s_cmp_lt_u32 s52, 0x100
	s_cbranch_scc0 .Lsched_store
	s_lshl_b32 s35, s52, 8
	s_or_b32 s35, s35, 0x5000000
	s_branch .Lsched_store
